# FIN: the final output rows (never re-read in the kernel) stored with the nt cache policy
# baseline (speedup 1.0000x reference)
.LBB0_1201:
	s_ashr_i32 s0, s25, 31
	s_lshr_b32 s0, s0, 20
	s_add_i32 s0, s25, s0
	s_ashr_i32 s40, s0, 12
	s_and_b32 s41, s0, 0xfffff000
	v_mad_i64_i32 v[50:51], s[0:1], s40, v62, v[18:19]
	s_mul_hi_i32 s0, s40, 0x1100
	s_mulk_i32 s40, 0x1100
	s_ashr_i32 s1, s41, 31
	s_sub_u32 s40, s40, s41
	s_subb_u32 s1, s0, s1
	s_add_u32 s0, s38, s40
	s_addc_u32 s1, s39, s1
	s_lshl_b64 s[0:1], s[0:1], 11
	global_load_dwordx4 v[34:37], v[50:51], off
	global_load_dwordx4 v[38:41], v[50:51], off offset:1024
	global_load_dwordx4 v[42:45], v[50:51], off offset:2048
	global_load_dwordx4 v[46:49], v[50:51], off offset:3072
	v_lshl_add_u64 v[50:51], v[20:21], 0, s[0:1]
	v_lshl_add_u64 v[52:53], v[22:23], 0, s[0:1]
	global_load_dwordx2 v[54:55], v[50:51], off
	global_load_dword v33, v[52:53], off
	global_load_dword v63, v[52:53], off offset:1024
	global_load_dwordx2 v[56:57], v[50:51], off offset:512
	global_load_dword v76, v[52:53], off offset:256
	global_load_dword v80, v[52:53], off offset:1280
	global_load_dwordx2 v[58:59], v[50:51], off offset:1024
	global_load_dword v86, v[52:53], off offset:512
	global_load_dword v90, v[52:53], off offset:1536
	global_load_dwordx2 v[64:65], v[50:51], off offset:1536
	global_load_dword v100, v[52:53], off offset:1792
	global_load_dword v96, v[52:53], off offset:768
	s_add_i32 s25, s25, s28
	s_add_u32 s38, s38, s28
	s_addc_u32 s39, s39, s29
	s_cmp_lt_i32 s25, 0x8000
	s_waitcnt vmcnt(11)
	v_lshlrev_b32_e32 v50, 16, v54
	v_and_b32_e32 v51, 0xffff0000, v54
	v_lshlrev_b32_e32 v52, 16, v55
	v_and_b32_e32 v53, 0xffff0000, v55
	s_waitcnt vmcnt(10)
	v_cvt_pk_f32_fp8_e32 v[54:55], v33
	v_cvt_pk_f32_fp8_sdwa v[66:67], v33 src0_sel:WORD_1
	s_waitcnt vmcnt(9)
	v_cvt_pk_f32_fp8_e32 v[68:69], v63
	v_cvt_pk_f32_fp8_sdwa v[70:71], v63 src0_sel:WORD_1
	s_waitcnt vmcnt(7)
	v_cvt_pk_f32_fp8_e32 v[74:75], v76
	v_cvt_pk_f32_fp8_sdwa v[76:77], v76 src0_sel:WORD_1
	s_waitcnt vmcnt(6)
	v_cvt_pk_f32_fp8_e32 v[78:79], v80
	v_cvt_pk_f32_fp8_sdwa v[80:81], v80 src0_sel:WORD_1
	s_waitcnt vmcnt(4)
	v_cvt_pk_f32_fp8_e32 v[84:85], v86
	v_cvt_pk_f32_fp8_sdwa v[86:87], v86 src0_sel:WORD_1
	s_waitcnt vmcnt(3)
	v_cvt_pk_f32_fp8_e32 v[88:89], v90
	v_cvt_pk_f32_fp8_sdwa v[90:91], v90 src0_sel:WORD_1
	s_waitcnt vmcnt(0)
	v_cvt_pk_f32_fp8_e32 v[94:95], v96
	v_cvt_pk_f32_fp8_sdwa v[96:97], v96 src0_sel:WORD_1
	v_cvt_pk_f32_fp8_e32 v[98:99], v100
	v_cvt_pk_f32_fp8_sdwa v[100:101], v100 src0_sel:WORD_1
	v_pk_mul_f32 v[36:37], v[36:37], s[6:7] op_sel_hi:[1,0]
	v_pk_mul_f32 v[34:35], v[34:35], s[6:7] op_sel_hi:[1,0]
	v_pk_mul_f32 v[40:41], v[40:41], s[6:7] op_sel_hi:[1,0]
	v_pk_mul_f32 v[38:39], v[38:39], s[6:7] op_sel_hi:[1,0]
	v_lshlrev_b32_e32 v72, 16, v56
	v_and_b32_e32 v73, 0xffff0000, v56
	v_lshlrev_b32_e32 v56, 16, v57
	v_and_b32_e32 v57, 0xffff0000, v57
	v_pk_add_f32 v[54:55], v[54:55], v[68:69]
	v_pk_add_f32 v[66:67], v[66:67], v[70:71]
	v_pk_add_f32 v[68:69], v[74:75], v[78:79]
	v_pk_add_f32 v[70:71], v[76:77], v[80:81]
	v_pk_fma_f32 v[34:35], v[34:35], v[54:55], v[50:51]
	v_pk_fma_f32 v[36:37], v[36:37], v[66:67], v[52:53]
	v_pk_fma_f32 v[38:39], v[38:39], v[68:69], v[72:73]
	v_pk_fma_f32 v[40:41], v[40:41], v[70:71], v[56:57]
	v_pk_mul_f32 v[42:43], v[42:43], s[6:7] op_sel_hi:[1,0]
	v_pk_mul_f32 v[44:45], v[44:45], s[6:7] op_sel_hi:[1,0]
	v_pk_mul_f32 v[48:49], v[48:49], s[6:7] op_sel_hi:[1,0]
	v_lshlrev_b32_e32 v82, 16, v58
	v_and_b32_e32 v83, 0xffff0000, v58
	v_lshlrev_b32_e32 v58, 16, v59
	v_and_b32_e32 v59, 0xffff0000, v59
	v_lshlrev_b32_e32 v92, 16, v64
	v_and_b32_e32 v93, 0xffff0000, v64
	v_lshlrev_b32_e32 v64, 16, v65
	v_and_b32_e32 v65, 0xffff0000, v65
	v_pk_add_f32 v[74:75], v[84:85], v[88:89]
	v_pk_add_f32 v[76:77], v[86:87], v[90:91]
	v_pk_add_f32 v[80:81], v[96:97], v[100:101]
	v_pk_mul_f32 v[50:51], v[36:37], v[36:37]
	v_pk_mul_f32 v[52:53], v[34:35], v[34:35]
	v_pk_mul_f32 v[54:55], v[40:41], v[40:41]
	v_pk_mul_f32 v[56:57], v[38:39], v[38:39]
	v_pk_mul_f32 v[46:47], v[46:47], s[6:7] op_sel_hi:[1,0]
	v_pk_add_f32 v[78:79], v[94:95], v[98:99]
	v_pk_fma_f32 v[44:45], v[44:45], v[76:77], v[58:59]
	v_pk_fma_f32 v[42:43], v[42:43], v[74:75], v[82:83]
	v_pk_fma_f32 v[48:49], v[48:49], v[80:81], v[64:65]
	v_pk_mov_b32 v[66:67], v[52:53], v[50:51] op_sel:[1,0]
	v_mov_b32_e32 v53, v51
	v_pk_mov_b32 v[50:51], v[56:57], v[54:55] op_sel:[1,0]
	v_mov_b32_e32 v57, v55
	v_pk_fma_f32 v[46:47], v[46:47], v[78:79], v[92:93]
	v_mul_f32_e32 v65, v48, v48
	v_mul_f32_e32 v58, v43, v43
	v_mul_f32_e32 v64, v45, v45
	v_pk_add_f32 v[52:53], v[66:67], v[52:53]
	v_pk_add_f32 v[50:51], v[50:51], v[56:57]
	v_mul_f32_e32 v33, v46, v46
	v_mul_f32_e32 v63, v47, v47
	v_mul_f32_e32 v68, v49, v49
	v_pk_fma_f32 v[54:55], v[42:43], v[42:43], v[58:59] op_sel_hi:[1,1,0]
	v_pk_fma_f32 v[58:59], v[44:45], v[44:45], v[64:65] op_sel_hi:[1,1,0]
	v_pk_add_f32 v[52:53], v[52:53], v[52:53] op_sel:[0,1] op_sel_hi:[1,0]
	v_pk_add_f32 v[50:51], v[50:51], v[50:51] op_sel:[0,1] op_sel_hi:[1,0]
	v_mov_b32_e32 v55, v65
	v_mov_b32_e32 v59, v68
	v_mov_b32_e32 v53, v33
	v_mov_b32_e32 v51, v63
	v_pk_add_f32 v[54:55], v[54:55], v[58:59]
	v_pk_add_f32 v[50:51], v[52:53], v[50:51]
	s_nop 0
	v_pk_add_f32 v[50:51], v[50:51], v[54:55]
	s_nop 0
	v_add_f32_e32 v33, v50, v51
	s_waitcnt lgkmcnt(0)
	s_nop 1
	v_add_f32_dpp v33, v33, v33 quad_perm:[1,0,3,2] row_mask:0xf bank_mask:0xf
	s_waitcnt lgkmcnt(0)
	s_nop 1
	v_add_f32_dpp v33, v33, v33 quad_perm:[2,3,0,1] row_mask:0xf bank_mask:0xf
	s_waitcnt lgkmcnt(0)
	s_nop 1
	v_add_f32_dpp v33, v33, v33 row_half_mirror row_mask:0xf bank_mask:0xf
	s_waitcnt lgkmcnt(0)
	s_nop 1
	v_add_f32_dpp v33, v33, v33 row_mirror row_mask:0xf bank_mask:0xf
	s_waitcnt lgkmcnt(0)
	s_nop 1
	v_add_f32_dpp v33, v33, v33 row_bcast:15 row_mask:0xa bank_mask:0xf
	s_waitcnt lgkmcnt(0)
	s_nop 1
	v_add_f32_dpp v33, v33, v33 row_bcast:31 row_mask:0xc bank_mask:0xf
	s_nop 0
	v_readlane_b32 s101, v33, 63
	s_nop 1
	v_mov_b32_e32 v33, s101
	v_fmamk_f32 v33, v33, 0x3a800000, v60
	v_mul_f32_e32 v50, 0x4f800000, v33
	v_cmp_gt_f32_e32 vcc, s33, v33
	s_nop 1
	v_cndmask_b32_e32 v33, v33, v50, vcc
	v_sqrt_f32_e32 v50, v33
	s_nop 0
	v_add_u32_e32 v51, -1, v50
	v_add_u32_e32 v52, 1, v50
	v_fma_f32 v53, -v51, v50, v33
	v_fma_f32 v54, -v52, v50, v33
	v_cmp_ge_f32_e64 s[0:1], 0, v53
	s_nop 1
	v_cndmask_b32_e64 v50, v50, v51, s[0:1]
	v_cmp_lt_f32_e64 s[0:1], 0, v54
	s_nop 1
	v_cndmask_b32_e64 v50, v50, v52, s[0:1]
	v_mul_f32_e32 v51, 0x37800000, v50
	v_cndmask_b32_e32 v50, v50, v51, vcc
	v_cmp_class_f32_e32 vcc, v33, v61
	s_nop 1
	v_cndmask_b32_e32 v33, v50, v33, vcc
	v_div_scale_f32 v50, s[0:1], v33, v33, 1.0
	v_rcp_f32_e32 v52, v50
	v_div_scale_f32 v51, vcc, 1.0, v33, 1.0
	v_fma_f32 v53, -v50, v52, 1.0
	v_fmac_f32_e32 v52, v53, v52
	v_mul_f32_e32 v53, v51, v52
	v_fma_f32 v54, -v50, v53, v51
	v_fmac_f32_e32 v53, v54, v52
	v_fma_f32 v50, -v50, v53, v51
	v_div_fmas_f32 v50, v50, v52, v53
	v_div_fixup_f32 v50, v50, v33, 1.0
	v_pk_mul_f32 v[34:35], v[50:51], v[34:35] op_sel_hi:[0,1]
	v_pk_mul_f32 v[36:37], v[50:51], v[36:37] op_sel_hi:[0,1]
	v_pk_mul_f32 v[38:39], v[50:51], v[38:39] op_sel_hi:[0,1]
	v_pk_mul_f32 v[40:41], v[50:51], v[40:41] op_sel_hi:[0,1]
	v_pk_mul_f32 v[42:43], v[50:51], v[42:43] op_sel_hi:[0,1]
	v_pk_mul_f32 v[44:45], v[50:51], v[44:45] op_sel_hi:[0,1]
	v_pk_mul_f32 v[46:47], v[50:51], v[46:47] op_sel_hi:[0,1]
	v_pk_mul_f32 v[48:49], v[50:51], v[48:49] op_sel_hi:[0,1]
	v_pk_mul_f32 v[36:37], v[36:37], v[2:3]
	v_pk_mul_f32 v[34:35], v[34:35], v[0:1]
	v_pk_mul_f32 v[40:41], v[40:41], v[6:7]
	v_pk_mul_f32 v[38:39], v[38:39], v[4:5]
	v_pk_mul_f32 v[44:45], v[44:45], v[10:11]
	v_pk_mul_f32 v[42:43], v[42:43], v[8:9]
	v_pk_mul_f32 v[48:49], v[48:49], v[14:15]
	v_pk_mul_f32 v[46:47], v[46:47], v[12:13]
	global_store_dwordx4 v[24:25], v[34:37], off offset:-2048 nt
	global_store_dwordx4 v[24:25], v[38:41], off offset:-1024 nt
	global_store_dwordx4 v[24:25], v[42:45], off nt
	global_store_dwordx4 v[24:25], v[46:49], off offset:1024 nt
	v_lshl_add_u64 v[24:25], v[24:25], 0, s[30:31]
	s_cbranch_scc1 .LBB0_1201

.LBB0_1205:
	s_waitcnt vmcnt(11)
	v_cvt_pk_f32_fp8_e32 v[86:87], v83
	v_cvt_pk_f32_fp8_sdwa v[88:89], v83 src0_sel:WORD_1
	s_waitcnt vmcnt(10)
	v_cvt_pk_f32_fp8_e32 v[90:91], v82
	v_cvt_pk_f32_fp8_sdwa v[82:83], v82 src0_sel:WORD_1
	v_lshlrev_b32_e32 v84, 16, v58
	v_and_b32_e32 v85, 0xffff0000, v58
	v_lshlrev_b32_e32 v58, 16, v59
	v_and_b32_e32 v59, 0xffff0000, v59
	v_pk_add_f32 v[86:87], v[86:87], v[90:91]
	v_pk_add_f32 v[82:83], v[88:89], v[82:83]
	v_pk_fma_f32 v[84:85], v[34:35], v[86:87], v[84:85]
	v_pk_fma_f32 v[58:59], v[32:33], v[82:83], v[58:59]
	v_pk_mul_f32 v[86:87], v[84:85], v[84:85]
	v_pk_mul_f32 v[82:83], v[58:59], v[58:59]
	s_waitcnt vmcnt(9)
	v_cvt_pk_f32_fp8_sdwa v[90:91], v81 src0_sel:WORD_1
	v_pk_mov_b32 v[88:89], v[86:87], v[82:83] op_sel:[1,0]
	v_mov_b32_e32 v87, v83
	v_pk_add_f32 v[82:83], v[88:89], v[86:87]
	v_cvt_pk_f32_fp8_e32 v[88:89], v81
	s_waitcnt vmcnt(8)
	v_cvt_pk_f32_fp8_e32 v[92:93], v80
	v_cvt_pk_f32_fp8_sdwa v[80:81], v80 src0_sel:WORD_1
	v_lshlrev_b32_e32 v86, 16, v56
	v_and_b32_e32 v87, 0xffff0000, v56
	v_lshlrev_b32_e32 v56, 16, v57
	v_and_b32_e32 v57, 0xffff0000, v57
	v_pk_add_f32 v[88:89], v[88:89], v[92:93]
	v_pk_add_f32 v[80:81], v[90:91], v[80:81]
	v_pk_fma_f32 v[86:87], v[38:39], v[88:89], v[86:87]
	v_pk_fma_f32 v[56:57], v[36:37], v[80:81], v[56:57]
	v_pk_mul_f32 v[88:89], v[86:87], v[86:87]
	v_pk_mul_f32 v[80:81], v[56:57], v[56:57]
	s_waitcnt vmcnt(6)
	v_cvt_pk_f32_fp8_e32 v[94:95], v78
	v_pk_mov_b32 v[90:91], v[88:89], v[80:81] op_sel:[1,0]
	v_mov_b32_e32 v89, v81
	v_pk_add_f32 v[80:81], v[90:91], v[88:89]
	v_cvt_pk_f32_fp8_e32 v[90:91], v79
	v_cvt_pk_f32_fp8_sdwa v[92:93], v79 src0_sel:WORD_1
	v_cvt_pk_f32_fp8_sdwa v[78:79], v78 src0_sel:WORD_1
	v_lshlrev_b32_e32 v88, 16, v54
	v_and_b32_e32 v89, 0xffff0000, v54
	v_pk_add_f32 v[90:91], v[90:91], v[94:95]
	s_waitcnt vmcnt(5)
	v_cvt_pk_f32_fp8_e32 v[94:95], v16
	v_pk_fma_f32 v[88:89], v[42:43], v[90:91], v[88:89]
	s_waitcnt vmcnt(4)
	v_cvt_pk_f32_fp8_e32 v[90:91], v77
	v_pk_add_f32 v[78:79], v[92:93], v[78:79]
	v_cvt_pk_f32_fp8_sdwa v[92:93], v77 src0_sel:WORD_1
	v_cvt_pk_f32_fp8_sdwa v[96:97], v16 src0_sel:WORD_1
	v_lshlrev_b32_e32 v54, 16, v55
	v_and_b32_e32 v55, 0xffff0000, v55
	v_pk_fma_f32 v[78:79], v[40:41], v[78:79], v[54:55]
	v_lshlrev_b32_e32 v54, 16, v52
	v_and_b32_e32 v55, 0xffff0000, v52
	v_pk_add_f32 v[90:91], v[90:91], v[94:95]
	v_lshlrev_b32_e32 v52, 16, v53
	v_and_b32_e32 v53, 0xffff0000, v53
	v_pk_add_f32 v[92:93], v[92:93], v[96:97]
	v_pk_fma_f32 v[90:91], v[46:47], v[90:91], v[54:55]
	v_pk_fma_f32 v[92:93], v[44:45], v[92:93], v[52:53]
	v_mul_f32_e32 v16, v90, v90
	v_mul_f32_e32 v77, v91, v91
	v_pk_add_f32 v[52:53], v[82:83], v[82:83] op_sel:[0,1] op_sel_hi:[1,0]
	v_pk_add_f32 v[54:55], v[80:81], v[80:81] op_sel:[0,1] op_sel_hi:[1,0]
	v_mov_b32_e32 v53, v16
	v_mov_b32_e32 v55, v77
	v_mul_f32_e32 v16, v89, v89
	v_pk_add_f32 v[52:53], v[52:53], v[54:55]
	v_pk_fma_f32 v[54:55], v[88:89], v[88:89], v[16:17] op_sel_hi:[1,1,0]
	v_mul_f32_e32 v16, v79, v79
	v_mul_f32_e32 v94, v92, v92
	v_mul_f32_e32 v95, v93, v93
	v_pk_fma_f32 v[80:81], v[78:79], v[78:79], v[16:17] op_sel_hi:[1,1,0]
	v_mov_b32_e32 v55, v94
	v_mov_b32_e32 v81, v95
	v_pk_add_f32 v[54:55], v[54:55], v[80:81]
	s_add_i32 s21, s21, 2
	v_pk_add_f32 v[52:53], v[52:53], v[54:55]
	v_lshl_add_u64 v[30:31], v[30:31], 0, s[14:15]
	v_add_f32_e32 v16, v52, v53
	v_lshl_add_u64 v[50:51], v[50:51], 0, s[14:15]
	s_waitcnt lgkmcnt(0)
	s_nop 1
	v_add_f32_dpp v16, v16, v16 quad_perm:[1,0,3,2] row_mask:0xf bank_mask:0xf
	s_waitcnt lgkmcnt(0)
	s_nop 1
	v_add_f32_dpp v16, v16, v16 quad_perm:[2,3,0,1] row_mask:0xf bank_mask:0xf
	s_waitcnt lgkmcnt(0)
	s_nop 1
	v_add_f32_dpp v16, v16, v16 row_half_mirror row_mask:0xf bank_mask:0xf
	s_waitcnt lgkmcnt(0)
	s_nop 1
	v_add_f32_dpp v16, v16, v16 row_mirror row_mask:0xf bank_mask:0xf
	s_waitcnt lgkmcnt(0)
	s_nop 1
	v_add_f32_dpp v16, v16, v16 row_bcast:15 row_mask:0xa bank_mask:0xf
	s_waitcnt lgkmcnt(0)
	s_nop 1
	v_add_f32_dpp v16, v16, v16 row_bcast:31 row_mask:0xc bank_mask:0xf
	s_nop 0
	v_readlane_b32 s101, v16, 63
	s_nop 1
	v_mov_b32_e32 v16, s101
	v_fmamk_f32 v16, v16, 0x3a800000, v60
	v_mul_f32_e32 v52, 0x4f800000, v16
	v_cmp_gt_f32_e32 vcc, s33, v16
	s_nop 1
	v_cndmask_b32_e32 v16, v16, v52, vcc
	v_sqrt_f32_e32 v52, v16
	s_nop 0
	v_add_u32_e32 v53, -1, v52
	v_fma_f32 v54, -v53, v52, v16
	v_cmp_ge_f32_e64 s[0:1], 0, v54
	v_add_u32_e32 v54, 1, v52
	s_nop 0
	v_cndmask_b32_e64 v53, v52, v53, s[0:1]
	v_fma_f32 v52, -v54, v52, v16
	v_cmp_lt_f32_e64 s[0:1], 0, v52
	s_nop 1
	v_cndmask_b32_e64 v52, v53, v54, s[0:1]
	v_mul_f32_e32 v53, 0x37800000, v52
	v_cndmask_b32_e32 v52, v52, v53, vcc
	v_cmp_class_f32_e32 vcc, v16, v61
	s_nop 1
	v_cndmask_b32_e32 v16, v52, v16, vcc
	v_div_scale_f32 v52, s[0:1], v16, v16, 1.0
	v_rcp_f32_e32 v53, v52
	s_nop 0
	v_fma_f32 v54, -v52, v53, 1.0
	v_fmac_f32_e32 v53, v54, v53
	v_div_scale_f32 v54, vcc, 1.0, v16, 1.0
	v_mul_f32_e32 v55, v54, v53
	v_fma_f32 v77, -v52, v55, v54
	v_fmac_f32_e32 v55, v77, v53
	v_fma_f32 v52, -v52, v55, v54
	v_div_fmas_f32 v52, v52, v53, v55
	v_div_fixup_f32 v16, v52, v16, 1.0
	v_pk_mul_f32 v[52:53], v[16:17], v[84:85] op_sel_hi:[0,1]
	v_pk_mul_f32 v[54:55], v[16:17], v[58:59] op_sel_hi:[0,1]
	v_pk_mul_f32 v[54:55], v[54:55], v[2:3]
	v_pk_mul_f32 v[52:53], v[52:53], v[0:1]
	global_store_dwordx4 v[48:49], v[52:55], off offset:-3072 nt
	s_and_b64 vcc, exec, s[18:19]
	s_nop 0
	v_pk_mul_f32 v[52:53], v[16:17], v[86:87] op_sel_hi:[0,1]
	v_pk_mul_f32 v[54:55], v[16:17], v[56:57] op_sel_hi:[0,1]
	v_pk_mul_f32 v[54:55], v[54:55], v[6:7]
	v_pk_mul_f32 v[52:53], v[52:53], v[4:5]
	global_store_dwordx4 v[48:49], v[52:55], off offset:-2048 nt
	s_nop 1
	v_pk_mul_f32 v[52:53], v[16:17], v[88:89] op_sel_hi:[0,1]
	v_pk_mul_f32 v[54:55], v[16:17], v[78:79] op_sel_hi:[0,1]
	v_pk_mul_f32 v[54:55], v[54:55], v[10:11]
	v_pk_mul_f32 v[52:53], v[52:53], v[8:9]
	global_store_dwordx4 v[48:49], v[52:55], off offset:-1024 nt
	s_nop 1
	v_pk_mul_f32 v[52:53], v[16:17], v[90:91] op_sel_hi:[0,1]
	v_pk_mul_f32 v[54:55], v[16:17], v[92:93] op_sel_hi:[0,1]
	v_pk_mul_f32 v[54:55], v[54:55], v[14:15]
	v_pk_mul_f32 v[52:53], v[52:53], v[12:13]
	global_store_dwordx4 v[48:49], v[52:55], off nt
	v_lshl_add_u64 v[48:49], v[48:49], 0, s[16:17]
	s_cbranch_vccnz .LBB0_1197
.LBB0_1206:
	s_waitcnt vmcnt(11)
	v_cvt_pk_f32_fp8_e32 v[54:55], v66
	v_cvt_pk_f32_fp8_sdwa v[56:57], v66 src0_sel:WORD_1
	s_waitcnt vmcnt(10)
	v_cvt_pk_f32_fp8_e32 v[58:59], v69
	v_cvt_pk_f32_fp8_sdwa v[78:79], v69 src0_sel:WORD_1
	s_waitcnt vmcnt(3)
	v_lshlrev_b32_e32 v52, 16, v18
	v_and_b32_e32 v53, 0xffff0000, v18
	v_lshlrev_b32_e32 v80, 16, v19
	v_and_b32_e32 v81, 0xffff0000, v19
	v_pk_add_f32 v[54:55], v[54:55], v[58:59]
	v_pk_add_f32 v[56:57], v[56:57], v[78:79]
	v_pk_fma_f32 v[84:85], v[34:35], v[54:55], v[52:53]
	v_pk_fma_f32 v[86:87], v[32:33], v[56:57], v[80:81]
	v_pk_mul_f32 v[54:55], v[84:85], v[84:85]
	v_pk_mul_f32 v[52:53], v[86:87], v[86:87]
	v_cvt_pk_f32_fp8_sdwa v[58:59], v71 src0_sel:WORD_1
	v_pk_mov_b32 v[56:57], v[54:55], v[52:53] op_sel:[1,0]
	v_mov_b32_e32 v55, v53
	v_pk_add_f32 v[52:53], v[56:57], v[54:55]
	v_cvt_pk_f32_fp8_e32 v[56:57], v71
	v_cvt_pk_f32_fp8_e32 v[78:79], v72
	v_cvt_pk_f32_fp8_sdwa v[80:81], v72 src0_sel:WORD_1
	s_waitcnt vmcnt(2)
	v_lshlrev_b32_e32 v54, 16, v22
	v_and_b32_e32 v55, 0xffff0000, v22
	v_lshlrev_b32_e32 v82, 16, v23
	v_and_b32_e32 v83, 0xffff0000, v23
	v_pk_add_f32 v[56:57], v[56:57], v[78:79]
	v_pk_add_f32 v[58:59], v[58:59], v[80:81]
	v_pk_fma_f32 v[88:89], v[38:39], v[56:57], v[54:55]
	v_pk_fma_f32 v[90:91], v[36:37], v[58:59], v[82:83]
	v_pk_mul_f32 v[56:57], v[88:89], v[88:89]
	v_pk_mul_f32 v[54:55], v[90:91], v[90:91]
	v_cvt_pk_f32_fp8_e32 v[80:81], v74
	v_pk_mov_b32 v[58:59], v[56:57], v[54:55] op_sel:[1,0]
	v_mov_b32_e32 v57, v55
	v_pk_add_f32 v[54:55], v[58:59], v[56:57]
	v_cvt_pk_f32_fp8_e32 v[58:59], v73
	v_cvt_pk_f32_fp8_sdwa v[78:79], v73 src0_sel:WORD_1
	v_cvt_pk_f32_fp8_sdwa v[82:83], v74 src0_sel:WORD_1
	s_waitcnt vmcnt(1)
	v_lshlrev_b32_e32 v56, 16, v24
	v_and_b32_e32 v57, 0xffff0000, v24
	v_pk_add_f32 v[58:59], v[58:59], v[80:81]
	v_cvt_pk_f32_fp8_e32 v[80:81], v75
	v_pk_fma_f32 v[94:95], v[42:43], v[58:59], v[56:57]
	v_cvt_pk_f32_fp8_e32 v[58:59], v76
	v_lshlrev_b32_e32 v92, 16, v25
	v_and_b32_e32 v93, 0xffff0000, v25
	v_pk_add_f32 v[78:79], v[78:79], v[82:83]
	v_cvt_pk_f32_fp8_sdwa v[82:83], v75 src0_sel:WORD_1
	v_pk_fma_f32 v[92:93], v[40:41], v[78:79], v[92:93]
	v_cvt_pk_f32_fp8_sdwa v[78:79], v76 src0_sel:WORD_1
	s_waitcnt vmcnt(0)
	v_lshlrev_b32_e32 v56, 16, v26
	v_and_b32_e32 v57, 0xffff0000, v26
	v_pk_add_f32 v[58:59], v[58:59], v[80:81]
	v_lshlrev_b32_e32 v96, 16, v27
	v_pk_fma_f32 v[98:99], v[46:47], v[58:59], v[56:57]
	v_and_b32_e32 v97, 0xffff0000, v27
	v_pk_add_f32 v[78:79], v[78:79], v[82:83]
	v_mul_f32_e32 v16, v98, v98
	v_mul_f32_e32 v56, v99, v99
	v_pk_add_f32 v[52:53], v[52:53], v[52:53] op_sel:[0,1] op_sel_hi:[1,0]
	v_pk_add_f32 v[54:55], v[54:55], v[54:55] op_sel:[0,1] op_sel_hi:[1,0]
	v_pk_fma_f32 v[96:97], v[44:45], v[78:79], v[96:97]
	v_mov_b32_e32 v53, v16
	v_mov_b32_e32 v55, v56
	v_mul_f32_e32 v16, v95, v95
	v_mul_f32_e32 v57, v96, v96
	v_pk_add_f32 v[52:53], v[52:53], v[54:55]
	v_pk_fma_f32 v[54:55], v[94:95], v[94:95], v[16:17] op_sel_hi:[1,1,0]
	v_mul_f32_e32 v16, v93, v93
	v_mul_f32_e32 v58, v97, v97
	v_mov_b32_e32 v55, v57
	v_pk_fma_f32 v[56:57], v[92:93], v[92:93], v[16:17] op_sel_hi:[1,1,0]
	s_cmp_gt_u32 s21, 13
	v_mov_b32_e32 v57, v58
	v_pk_add_f32 v[54:55], v[54:55], v[56:57]
	s_cselect_b64 s[18:19], -1, 0
	v_pk_add_f32 v[52:53], v[52:53], v[54:55]
	s_nop 0
	v_add_f32_e32 v16, v52, v53
	ds_bpermute_b32 v52, v63, v16
	s_waitcnt lgkmcnt(0)
	v_add_f32_e32 v16, v16, v52
	ds_bpermute_b32 v52, v64, v16
	s_waitcnt lgkmcnt(0)
	v_add_f32_e32 v16, v16, v52
	ds_bpermute_b32 v77, v65, v16
	global_load_dwordx2 v[58:59], v[50:51], off offset:-1024
	global_load_dwordx2 v[56:57], v[50:51], off offset:-512
	global_load_dwordx2 v[54:55], v[50:51], off
	global_load_dwordx2 v[52:53], v[50:51], off offset:512
	s_waitcnt lgkmcnt(0)
	v_add_f32_e32 v100, v16, v77
	global_load_dword v83, v[30:31], off offset:-1024
	global_load_dword v82, v[30:31], off
	global_load_dword v81, v[30:31], off offset:-768
	global_load_dword v80, v[30:31], off offset:256
	global_load_dword v79, v[30:31], off offset:-512
	global_load_dword v78, v[30:31], off offset:512
	global_load_dword v16, v[30:31], off offset:768
	global_load_dword v77, v[30:31], off offset:-256
	ds_bpermute_b32 v101, v67, v100
	s_waitcnt lgkmcnt(0)
	v_add_f32_e32 v100, v100, v101
	ds_bpermute_b32 v101, v68, v100
	s_waitcnt lgkmcnt(0)
	v_add_f32_e32 v100, v100, v101
	ds_bpermute_b32 v101, v70, v100
	s_waitcnt lgkmcnt(0)
	v_add_f32_e32 v100, v100, v101
	v_fmamk_f32 v100, v100, 0x3a800000, v60
	v_mul_f32_e32 v101, 0x4f800000, v100
	v_cmp_gt_f32_e32 vcc, s33, v100
	s_nop 1
	v_cndmask_b32_e32 v100, v100, v101, vcc
	v_sqrt_f32_e32 v101, v100
	s_nop 0
	v_add_u32_e32 v102, -1, v101
	v_fma_f32 v103, -v102, v101, v100
	v_cmp_ge_f32_e64 s[0:1], 0, v103
	v_add_u32_e32 v103, 1, v101
	s_nop 0
	v_cndmask_b32_e64 v102, v101, v102, s[0:1]
	v_fma_f32 v101, -v103, v101, v100
	v_cmp_lt_f32_e64 s[0:1], 0, v101
	s_nop 1
	v_cndmask_b32_e64 v101, v102, v103, s[0:1]
	v_mul_f32_e32 v102, 0x37800000, v101
	v_cndmask_b32_e32 v101, v101, v102, vcc
	v_cmp_class_f32_e32 vcc, v100, v61
	s_nop 1
	v_cndmask_b32_e32 v100, v101, v100, vcc
	v_div_scale_f32 v101, s[0:1], v100, v100, 1.0
	v_rcp_f32_e32 v102, v101
	s_nop 0
	v_fma_f32 v103, -v101, v102, 1.0
	v_fmac_f32_e32 v102, v103, v102
	v_div_scale_f32 v103, vcc, 1.0, v100, 1.0
	v_mul_f32_e32 v104, v103, v102
	v_fma_f32 v105, -v101, v104, v103
	v_fmac_f32_e32 v104, v105, v102
	v_fma_f32 v101, -v101, v104, v103
	v_div_fmas_f32 v101, v101, v102, v104
	v_div_fixup_f32 v100, v101, v100, 1.0
	v_pk_mul_f32 v[84:85], v[100:101], v[84:85] op_sel_hi:[0,1]
	v_pk_mul_f32 v[86:87], v[100:101], v[86:87] op_sel_hi:[0,1]
	v_add_co_u32_e32 v102, vcc, s7, v48
	v_pk_mul_f32 v[86:87], v[86:87], v[2:3]
	v_pk_mul_f32 v[84:85], v[84:85], v[0:1]
	v_addc_co_u32_e32 v103, vcc, -1, v49, vcc
	global_store_dwordx4 v[102:103], v[84:87], off offset:-3072 nt
	s_and_b64 vcc, exec, s[18:19]
	s_nop 0
	v_pk_mul_f32 v[84:85], v[100:101], v[88:89] op_sel_hi:[0,1]
	v_pk_mul_f32 v[86:87], v[100:101], v[90:91] op_sel_hi:[0,1]
	v_pk_mul_f32 v[86:87], v[86:87], v[6:7]
	v_pk_mul_f32 v[84:85], v[84:85], v[4:5]
	global_store_dwordx4 v[102:103], v[84:87], off offset:-2048 nt
	s_nop 1
	v_pk_mul_f32 v[84:85], v[100:101], v[94:95] op_sel_hi:[0,1]
	v_pk_mul_f32 v[86:87], v[100:101], v[92:93] op_sel_hi:[0,1]
	v_pk_mul_f32 v[86:87], v[86:87], v[10:11]
	v_pk_mul_f32 v[84:85], v[84:85], v[8:9]
	global_store_dwordx4 v[102:103], v[84:87], off offset:-1024 nt
	s_nop 1
	v_pk_mul_f32 v[84:85], v[100:101], v[98:99] op_sel_hi:[0,1]
	v_pk_mul_f32 v[86:87], v[100:101], v[96:97] op_sel_hi:[0,1]
	v_pk_mul_f32 v[86:87], v[86:87], v[14:15]
	v_pk_mul_f32 v[84:85], v[84:85], v[12:13]
	global_store_dwordx4 v[48:49], v[84:87], off offset:-4096 nt
	s_cbranch_vccnz .LBB0_1205
	s_add_i32 s0, s20, s21
	s_ashr_i32 s1, s0, 31
	s_add_u32 s0, s24, s0
	s_addc_u32 s1, s25, s1
	s_lshl_b64 s[0:1], s[0:1], 11
	v_lshl_add_u64 v[84:85], v[28:29], 0, s[0:1]
	v_lshl_add_u64 v[86:87], v[20:21], 0, s[0:1]
	global_load_dwordx2 v[18:19], v[84:85], off
	global_load_dwordx2 v[22:23], v[84:85], off offset:512
	global_load_dwordx2 v[24:25], v[84:85], off offset:1024
	global_load_dwordx2 v[26:27], v[84:85], off offset:1536
	global_load_dword v66, v[86:87], off
	global_load_dword v69, v[86:87], off offset:1024
	global_load_dword v71, v[86:87], off offset:256
	global_load_dword v72, v[86:87], off offset:1280
	global_load_dword v73, v[86:87], off offset:512
	global_load_dword v74, v[86:87], off offset:1536
	global_load_dword v75, v[86:87], off offset:1792
	global_load_dword v76, v[86:87], off offset:768
	s_branch .LBB0_1205
